# full-head attention epilogue: output tile staged through LDS and written as 8 whole-row dwordx4 stores per wave instead of 64 two-byte stores; on top of GEMM2-epilogue/router/combine/diff-combine load
# speedup vs baseline: 1.0024x; 1.0024x over previous
; __device__ __forceinline__ bf16_t f2bf(float f) { unsigned u = __float_as_uint(f); return (bf16_t)((u + 0x7fffu + ((u >> 16) & 1u)) >> 16); }
; __device__ __forceinline__ int crow(int r, int hi) { return (r & 3) + 8 * (r >> 2) + 4 * hi; }
; template <bool HALF> __device__ __forceinline__ void dense_body(const bf16_t* __restrict__ Qb, const bf16_t* __restrict__ Kh, const bf16_t* __restrict__ Vh, ...
;     ...
;   if (hi == 0) li_l[r32] = l_reg; asm volatile("s_waitcnt lgkmcnt(0)" ::: "memory");
;   float rli[16];
; #pragma unroll
;   for (int r = 0; r < 16; ++r) rli[r] = __builtin_amdgcn_rcpf(li_l[crow(r, hi)]);
;   int r32e = r32, hie = hi, wide = wid; asm volatile("" : "+v"(r32e), "+v"(hie), "+v"(wide));
;   if (Obf) {
; #pragma unroll
;     for (int r = 0; r < 16; ++r) { const unsigned ob = (unsigned)((wide * QBLK + crow(r, hie)) * DM + r32e);
; #pragma unroll
;       for (int d0 = 0; d0 < 4; ++d0) Obf[ob + d0 * 32] = f2bf(o[d0][r] * rli[r]); }
.LBB0_415:
	s_or_b64 exec, exec, s[6:7]
	s_waitcnt lgkmcnt(0)
	v_add_u32_e32 v64, v200, v96
	ds_read_b128 v[66:69], v64 offset:64
	ds_read_b128 v[70:73], v64 offset:96
	ds_read_b128 v[74:77], v64
	ds_read_b128 v[78:81], v64 offset:32
	s_lshl_b32 s2, s19, 12
	s_add_u32 s4, s0, s2
	s_addc_u32 s6, s1, 0
	s_ashr_i32 s19, s18, 31
	s_lshl_b64 s[2:3], s[18:19], 1
	s_add_u32 s2, s4, s2
	s_addc_u32 s3, s6, s3
	s_add_u32 s18, s2, 0x2d814400
	s_addc_u32 s19, s3, 0
	v_lshrrev_b32_e32 v83, 2, v198
	v_add_u32_e32 v83, v83, v198
	v_lshlrev_b32_e32 v83, 13, v83
	v_add_u32_e32 v83, 0x8000, v83
	v_lshl_add_u32 v86, v199, 10, v83
	v_lshl_add_u32 v86, v197, 1, v86
	v_lshl_add_u32 v85, v199, 5, v197
	v_lshl_add_u32 v87, v85, 4, v83
	v_lshrrev_b32_e32 v84, 4, v85
	v_lshlrev_b32_e32 v88, 17, v198
	v_lshl_add_u32 v88, v84, 12, v88
	v_and_b32_e32 v84, 15, v85
	v_lshl_add_u32 v88, v84, 4, v88
	s_waitcnt lgkmcnt(0)
	v_rcp_f32_e32 v74, v74
	v_rcp_f32_e32 v75, v75
	v_rcp_f32_e32 v76, v76
	v_rcp_f32_e32 v77, v77
	v_rcp_f32_e32 v78, v78
	v_rcp_f32_e32 v79, v79
	v_rcp_f32_e32 v80, v80
	v_rcp_f32_e32 v81, v81
	v_rcp_f32_e32 v66, v66
	v_rcp_f32_e32 v67, v67
	v_rcp_f32_e32 v68, v68
	v_rcp_f32_e32 v69, v69
	v_rcp_f32_e32 v70, v70
	v_rcp_f32_e32 v71, v71
	v_rcp_f32_e32 v72, v72
	v_rcp_f32_e32 v73, v73
	s_nop 0
	v_mul_f32_e32 v0, v0, v74
	v_bfe_u32 v82, v0, 16, 1
	v_add3_u32 v0, v0, v82, s86
	ds_write_b16_d16_hi v86, v0
	v_mul_f32_e32 v48, v48, v74
	v_bfe_u32 v82, v48, 16, 1
	v_add3_u32 v48, v48, v82, s86
	ds_write_b16_d16_hi v86, v48 offset:64
	v_mul_f32_e32 v32, v32, v74
	v_bfe_u32 v82, v32, 16, 1
	v_add3_u32 v32, v32, v82, s86
	ds_write_b16_d16_hi v86, v32 offset:128
	v_mul_f32_e32 v16, v16, v74
	v_bfe_u32 v82, v16, 16, 1
	v_add3_u32 v16, v16, v82, s86
	ds_write_b16_d16_hi v86, v16 offset:192
	v_mul_f32_e32 v1, v1, v75
	v_bfe_u32 v82, v1, 16, 1
	v_add3_u32 v1, v1, v82, s86
	ds_write_b16_d16_hi v86, v1 offset:256
	v_mul_f32_e32 v49, v49, v75
	v_bfe_u32 v82, v49, 16, 1
	v_add3_u32 v49, v49, v82, s86
	ds_write_b16_d16_hi v86, v49 offset:320
	v_mul_f32_e32 v33, v33, v75
	v_bfe_u32 v82, v33, 16, 1
	v_add3_u32 v33, v33, v82, s86
	ds_write_b16_d16_hi v86, v33 offset:384
	v_mul_f32_e32 v17, v17, v75
	v_bfe_u32 v82, v17, 16, 1
	v_add3_u32 v17, v17, v82, s86
	ds_write_b16_d16_hi v86, v17 offset:448
	v_mul_f32_e32 v2, v2, v76
	v_bfe_u32 v82, v2, 16, 1
	v_add3_u32 v2, v2, v82, s86
	ds_write_b16_d16_hi v86, v2 offset:512
	v_mul_f32_e32 v50, v50, v76
	v_bfe_u32 v82, v50, 16, 1
	v_add3_u32 v50, v50, v82, s86
	ds_write_b16_d16_hi v86, v50 offset:576
	v_mul_f32_e32 v34, v34, v76
	v_bfe_u32 v82, v34, 16, 1
	v_add3_u32 v34, v34, v82, s86
	ds_write_b16_d16_hi v86, v34 offset:640
	v_mul_f32_e32 v18, v18, v76
	v_bfe_u32 v82, v18, 16, 1
	v_add3_u32 v18, v18, v82, s86
	ds_write_b16_d16_hi v86, v18 offset:704
	v_mul_f32_e32 v3, v3, v77
	v_bfe_u32 v82, v3, 16, 1
	v_add3_u32 v3, v3, v82, s86
	ds_write_b16_d16_hi v86, v3 offset:768
	v_mul_f32_e32 v51, v51, v77
	v_bfe_u32 v82, v51, 16, 1
	v_add3_u32 v51, v51, v82, s86
	ds_write_b16_d16_hi v86, v51 offset:832
	v_mul_f32_e32 v35, v35, v77
	v_bfe_u32 v82, v35, 16, 1
	v_add3_u32 v35, v35, v82, s86
	ds_write_b16_d16_hi v86, v35 offset:896
	v_mul_f32_e32 v19, v19, v77
	v_bfe_u32 v82, v19, 16, 1
	v_add3_u32 v19, v19, v82, s86
	ds_write_b16_d16_hi v86, v19 offset:960
	v_mul_f32_e32 v4, v4, v78
	v_bfe_u32 v82, v4, 16, 1
	v_add3_u32 v4, v4, v82, s86
	ds_write_b16_d16_hi v86, v4 offset:2048
	v_mul_f32_e32 v52, v52, v78
	v_bfe_u32 v82, v52, 16, 1
	v_add3_u32 v52, v52, v82, s86
	ds_write_b16_d16_hi v86, v52 offset:2112
	v_mul_f32_e32 v36, v36, v78
	v_bfe_u32 v82, v36, 16, 1
	v_add3_u32 v36, v36, v82, s86
	ds_write_b16_d16_hi v86, v36 offset:2176
	v_mul_f32_e32 v20, v20, v78
	v_bfe_u32 v82, v20, 16, 1
	v_add3_u32 v20, v20, v82, s86
	ds_write_b16_d16_hi v86, v20 offset:2240
	v_mul_f32_e32 v5, v5, v79
	v_bfe_u32 v82, v5, 16, 1
	v_add3_u32 v5, v5, v82, s86
	ds_write_b16_d16_hi v86, v5 offset:2304
	v_mul_f32_e32 v53, v53, v79
	v_bfe_u32 v82, v53, 16, 1
	v_add3_u32 v53, v53, v82, s86
	ds_write_b16_d16_hi v86, v53 offset:2368
	v_mul_f32_e32 v37, v37, v79
	v_bfe_u32 v82, v37, 16, 1
	v_add3_u32 v37, v37, v82, s86
	ds_write_b16_d16_hi v86, v37 offset:2432
	v_mul_f32_e32 v21, v21, v79
	v_bfe_u32 v82, v21, 16, 1
	v_add3_u32 v21, v21, v82, s86
	ds_write_b16_d16_hi v86, v21 offset:2496
	v_mul_f32_e32 v6, v6, v80
	v_bfe_u32 v82, v6, 16, 1
	v_add3_u32 v6, v6, v82, s86
	ds_write_b16_d16_hi v86, v6 offset:2560
	v_mul_f32_e32 v54, v54, v80
	v_bfe_u32 v82, v54, 16, 1
	v_add3_u32 v54, v54, v82, s86
	ds_write_b16_d16_hi v86, v54 offset:2624
	v_mul_f32_e32 v38, v38, v80
	v_bfe_u32 v82, v38, 16, 1
	v_add3_u32 v38, v38, v82, s86
	ds_write_b16_d16_hi v86, v38 offset:2688
	v_mul_f32_e32 v22, v22, v80
	v_bfe_u32 v82, v22, 16, 1
	v_add3_u32 v22, v22, v82, s86
	ds_write_b16_d16_hi v86, v22 offset:2752
	v_mul_f32_e32 v7, v7, v81
	v_bfe_u32 v82, v7, 16, 1
	v_add3_u32 v7, v7, v82, s86
	ds_write_b16_d16_hi v86, v7 offset:2816
	v_mul_f32_e32 v55, v55, v81
	v_bfe_u32 v82, v55, 16, 1
	v_add3_u32 v55, v55, v82, s86
	ds_write_b16_d16_hi v86, v55 offset:2880
	v_mul_f32_e32 v39, v39, v81
	v_bfe_u32 v82, v39, 16, 1
	v_add3_u32 v39, v39, v82, s86
	ds_write_b16_d16_hi v86, v39 offset:2944
	v_mul_f32_e32 v23, v23, v81
	v_bfe_u32 v82, v23, 16, 1
	v_add3_u32 v23, v23, v82, s86
	ds_write_b16_d16_hi v86, v23 offset:3008
; __device__ __forceinline__ bf16_t f2bf(float f) { unsigned u = __float_as_uint(f); return (bf16_t)((u + 0x7fffu + ((u >> 16) & 1u)) >> 16); }
; __device__ __forceinline__ int crow(int r, int hi) { return (r & 3) + 8 * (r >> 2) + 4 * hi; }
; template <bool HALF> __device__ __forceinline__ void dense_body(const bf16_t* __restrict__ Qb, const bf16_t* __restrict__ Kh, const bf16_t* __restrict__ Vh, ...
;     ...
;   if (hi == 0) li_l[r32] = l_reg; asm volatile("s_waitcnt lgkmcnt(0)" ::: "memory");
;   float rli[16];
; #pragma unroll
;   for (int r = 0; r < 16; ++r) rli[r] = __builtin_amdgcn_rcpf(li_l[crow(r, hi)]);
;   int r32e = r32, hie = hi, wide = wid; asm volatile("" : "+v"(r32e), "+v"(hie), "+v"(wide));
;   if (Obf) {
; #pragma unroll
;     for (int r = 0; r < 16; ++r) { const unsigned ob = (unsigned)((wide * QBLK + crow(r, hie)) * DM + r32e);
; #pragma unroll
;       for (int d0 = 0; d0 < 4; ++d0) Obf[ob + d0 * 32] = f2bf(o[d0][r] * rli[r]); }
	v_mul_f32_e32 v8, v8, v66
	v_bfe_u32 v82, v8, 16, 1
	v_add3_u32 v8, v8, v82, s86
	ds_write_b16_d16_hi v86, v8 offset:4096
	v_mul_f32_e32 v56, v56, v66
	v_bfe_u32 v82, v56, 16, 1
	v_add3_u32 v56, v56, v82, s86
	ds_write_b16_d16_hi v86, v56 offset:4160
	v_mul_f32_e32 v40, v40, v66
	v_bfe_u32 v82, v40, 16, 1
	v_add3_u32 v40, v40, v82, s86
	ds_write_b16_d16_hi v86, v40 offset:4224
	v_mul_f32_e32 v24, v24, v66
	v_bfe_u32 v82, v24, 16, 1
	v_add3_u32 v24, v24, v82, s86
	ds_write_b16_d16_hi v86, v24 offset:4288
	v_mul_f32_e32 v9, v9, v67
	v_bfe_u32 v82, v9, 16, 1
	v_add3_u32 v9, v9, v82, s86
	ds_write_b16_d16_hi v86, v9 offset:4352
	v_mul_f32_e32 v57, v57, v67
	v_bfe_u32 v82, v57, 16, 1
	v_add3_u32 v57, v57, v82, s86
	ds_write_b16_d16_hi v86, v57 offset:4416
	v_mul_f32_e32 v41, v41, v67
	v_bfe_u32 v82, v41, 16, 1
	v_add3_u32 v41, v41, v82, s86
	ds_write_b16_d16_hi v86, v41 offset:4480
	v_mul_f32_e32 v25, v25, v67
	v_bfe_u32 v82, v25, 16, 1
	v_add3_u32 v25, v25, v82, s86
	ds_write_b16_d16_hi v86, v25 offset:4544
	v_mul_f32_e32 v10, v10, v68
	v_bfe_u32 v82, v10, 16, 1
	v_add3_u32 v10, v10, v82, s86
	ds_write_b16_d16_hi v86, v10 offset:4608
	v_mul_f32_e32 v58, v58, v68
	v_bfe_u32 v82, v58, 16, 1
	v_add3_u32 v58, v58, v82, s86
	ds_write_b16_d16_hi v86, v58 offset:4672
	v_mul_f32_e32 v42, v42, v68
	v_bfe_u32 v82, v42, 16, 1
	v_add3_u32 v42, v42, v82, s86
	ds_write_b16_d16_hi v86, v42 offset:4736
	v_mul_f32_e32 v26, v26, v68
	v_bfe_u32 v82, v26, 16, 1
	v_add3_u32 v26, v26, v82, s86
	ds_write_b16_d16_hi v86, v26 offset:4800
	v_mul_f32_e32 v11, v11, v69
	v_bfe_u32 v82, v11, 16, 1
	v_add3_u32 v11, v11, v82, s86
	ds_write_b16_d16_hi v86, v11 offset:4864
	v_mul_f32_e32 v59, v59, v69
	v_bfe_u32 v82, v59, 16, 1
	v_add3_u32 v59, v59, v82, s86
	ds_write_b16_d16_hi v86, v59 offset:4928
	v_mul_f32_e32 v43, v43, v69
	v_bfe_u32 v82, v43, 16, 1
	v_add3_u32 v43, v43, v82, s86
	ds_write_b16_d16_hi v86, v43 offset:4992
	v_mul_f32_e32 v27, v27, v69
	v_bfe_u32 v82, v27, 16, 1
	v_add3_u32 v27, v27, v82, s86
	ds_write_b16_d16_hi v86, v27 offset:5056
	v_mul_f32_e32 v12, v12, v70
	v_bfe_u32 v82, v12, 16, 1
	v_add3_u32 v12, v12, v82, s86
	ds_write_b16_d16_hi v86, v12 offset:6144
	v_mul_f32_e32 v60, v60, v70
	v_bfe_u32 v82, v60, 16, 1
	v_add3_u32 v60, v60, v82, s86
	ds_write_b16_d16_hi v86, v60 offset:6208
	v_mul_f32_e32 v44, v44, v70
	v_bfe_u32 v82, v44, 16, 1
	v_add3_u32 v44, v44, v82, s86
	ds_write_b16_d16_hi v86, v44 offset:6272
	v_mul_f32_e32 v28, v28, v70
	v_bfe_u32 v82, v28, 16, 1
	v_add3_u32 v28, v28, v82, s86
	ds_write_b16_d16_hi v86, v28 offset:6336
	v_mul_f32_e32 v13, v13, v71
	v_bfe_u32 v82, v13, 16, 1
	v_add3_u32 v13, v13, v82, s86
	ds_write_b16_d16_hi v86, v13 offset:6400
	v_mul_f32_e32 v61, v61, v71
	v_bfe_u32 v82, v61, 16, 1
	v_add3_u32 v61, v61, v82, s86
	ds_write_b16_d16_hi v86, v61 offset:6464
	v_mul_f32_e32 v45, v45, v71
	v_bfe_u32 v82, v45, 16, 1
	v_add3_u32 v45, v45, v82, s86
	ds_write_b16_d16_hi v86, v45 offset:6528
	v_mul_f32_e32 v29, v29, v71
	v_bfe_u32 v82, v29, 16, 1
	v_add3_u32 v29, v29, v82, s86
	ds_write_b16_d16_hi v86, v29 offset:6592
	v_mul_f32_e32 v14, v14, v72
	v_bfe_u32 v82, v14, 16, 1
	v_add3_u32 v14, v14, v82, s86
	ds_write_b16_d16_hi v86, v14 offset:6656
	v_mul_f32_e32 v62, v62, v72
	v_bfe_u32 v82, v62, 16, 1
	v_add3_u32 v62, v62, v82, s86
	ds_write_b16_d16_hi v86, v62 offset:6720
	v_mul_f32_e32 v46, v46, v72
	v_bfe_u32 v82, v46, 16, 1
	v_add3_u32 v46, v46, v82, s86
	ds_write_b16_d16_hi v86, v46 offset:6784
	v_mul_f32_e32 v30, v30, v72
	v_bfe_u32 v82, v30, 16, 1
	v_add3_u32 v30, v30, v82, s86
	ds_write_b16_d16_hi v86, v30 offset:6848
	v_mul_f32_e32 v15, v15, v73
	v_bfe_u32 v82, v15, 16, 1
	v_add3_u32 v15, v15, v82, s86
	ds_write_b16_d16_hi v86, v15 offset:6912
	v_mul_f32_e32 v63, v63, v73
	v_bfe_u32 v82, v63, 16, 1
	v_add3_u32 v63, v63, v82, s86
	ds_write_b16_d16_hi v86, v63 offset:6976
	v_mul_f32_e32 v47, v47, v73
	v_bfe_u32 v82, v47, 16, 1
	v_add3_u32 v47, v47, v82, s86
	ds_write_b16_d16_hi v86, v47 offset:7040
	v_mul_f32_e32 v31, v31, v73
	v_bfe_u32 v82, v31, 16, 1
	v_add3_u32 v31, v31, v82, s86
	ds_write_b16_d16_hi v86, v31 offset:7104
	s_waitcnt lgkmcnt(0)
	ds_read_b128 v[0:3], v87
	ds_read_b128 v[4:7], v87 offset:1024
	ds_read_b128 v[8:11], v87 offset:2048
	ds_read_b128 v[12:15], v87 offset:3072
	ds_read_b128 v[16:19], v87 offset:4096
	ds_read_b128 v[20:23], v87 offset:5120
	ds_read_b128 v[24:27], v87 offset:6144
	ds_read_b128 v[28:31], v87 offset:7168
	s_add_i32 s47, s47, s97
	s_waitcnt lgkmcnt(7)
	global_store_dwordx4 v88, v[0:3], s[18:19]
	v_add_u32_e32 v88, 0x4000, v88
	s_waitcnt lgkmcnt(6)
	global_store_dwordx4 v88, v[4:7], s[18:19]
	v_add_u32_e32 v88, 0x4000, v88
	s_waitcnt lgkmcnt(5)
	global_store_dwordx4 v88, v[8:11], s[18:19]
	v_add_u32_e32 v88, 0x4000, v88
	s_waitcnt lgkmcnt(4)
	global_store_dwordx4 v88, v[12:15], s[18:19]
	v_add_u32_e32 v88, 0x4000, v88
	s_waitcnt lgkmcnt(3)
	global_store_dwordx4 v88, v[16:19], s[18:19]
	v_add_u32_e32 v88, 0x4000, v88
	s_waitcnt lgkmcnt(2)
	global_store_dwordx4 v88, v[20:23], s[18:19]
	v_add_u32_e32 v88, 0x4000, v88
	s_waitcnt lgkmcnt(1)
	global_store_dwordx4 v88, v[24:27], s[18:19]
	v_add_u32_e32 v88, 0x4000, v88
	s_waitcnt lgkmcnt(0)
	global_store_dwordx4 v88, v[28:31], s[18:19]
	s_cmp_lt_i32 s47, s5
	s_waitcnt vmcnt(63) expcnt(7) lgkmcnt(15)
	s_barrier
	s_cbranch_scc0 .LBB0_443
